# more nt hints: final-phase loads/stores, P6 projection stores, residual-stream loads of the P8/P11/P14 epilogues
# baseline (speedup 1.0000x reference)
.LBB0_974:
	s_nop 0
	v_cndmask_b32_e64 v4, 0, 1, s[4:5]
	v_cmp_ne_u32_e64 s[38:39], 1, v4
	v_or_b32_e32 v4, s13, v180
	v_mad_u32_u24 v228, v4, s33, v2
	ds_read_b128 v[4:7], v228
	ds_read_b128 v[196:199], v228 offset:32
	ds_read_b128 v[204:207], v228 offset:64
	ds_read_b128 v[208:211], v228 offset:96
	ds_read_b128 v[212:215], v228 offset:128
	ds_read_b128 v[216:219], v228 offset:160
	ds_read_b128 v[220:223], v228 offset:192
	ds_read_b128 v[224:227], v228 offset:224
	s_waitcnt lgkmcnt(7)
	v_mfma_f32_32x32x16_bf16 v[20:35], v[36:39], v[4:7], 0
	v_mfma_f32_32x32x16_bf16 v[4:19], v[100:103], v[4:7], 0
	s_waitcnt lgkmcnt(6)
	v_mfma_f32_32x32x16_bf16 v[20:35], v[40:43], v[196:199], v[20:35]
	v_mfma_f32_32x32x16_bf16 v[4:19], v[104:107], v[196:199], v[4:19]
	s_waitcnt lgkmcnt(5)
	v_mfma_f32_32x32x16_bf16 v[20:35], v[44:47], v[204:207], v[20:35]
	v_mfma_f32_32x32x16_bf16 v[4:19], v[108:111], v[204:207], v[4:19]
	s_waitcnt lgkmcnt(4)
	v_mfma_f32_32x32x16_bf16 v[20:35], v[48:51], v[208:211], v[20:35]
	v_mfma_f32_32x32x16_bf16 v[4:19], v[112:115], v[208:211], v[4:19]
	s_waitcnt lgkmcnt(3)
	v_mfma_f32_32x32x16_bf16 v[20:35], v[52:55], v[212:215], v[20:35]
	v_mfma_f32_32x32x16_bf16 v[4:19], v[116:119], v[212:215], v[4:19]
	s_waitcnt lgkmcnt(2)
	v_mfma_f32_32x32x16_bf16 v[20:35], v[56:59], v[216:219], v[20:35]
	v_mfma_f32_32x32x16_bf16 v[4:19], v[120:123], v[216:219], v[4:19]
	s_waitcnt lgkmcnt(1)
	v_mfma_f32_32x32x16_bf16 v[20:35], v[60:63], v[220:223], v[20:35]
	v_mfma_f32_32x32x16_bf16 v[4:19], v[124:127], v[220:223], v[4:19]
	s_waitcnt lgkmcnt(0)
	v_mfma_f32_32x32x16_bf16 v[20:35], v[64:67], v[224:227], v[20:35]
	v_mfma_f32_32x32x16_bf16 v[4:19], v[128:131], v[224:227], v[4:19]
	ds_read_b128 v[196:199], v228 offset:256
	ds_read_b128 v[204:207], v228 offset:288
	ds_read_b128 v[208:211], v228 offset:320
	ds_read_b128 v[212:215], v228 offset:352
	ds_read_b128 v[216:219], v228 offset:384
	ds_read_b128 v[220:223], v228 offset:416
	ds_read_b128 v[224:227], v228 offset:448
	ds_read_b128 v[228:231], v228 offset:480
	s_waitcnt lgkmcnt(7)
	v_mfma_f32_32x32x16_bf16 v[20:35], v[68:71], v[196:199], v[20:35]
	s_mov_b64 s[4:5], 0
	v_mfma_f32_32x32x16_bf16 v[4:19], v[132:135], v[196:199], v[4:19]
	v_or_b32_e32 v196, s13, v194
	v_mov_b32_e32 v197, v195
	s_mov_b32 s13, 32
	s_waitcnt lgkmcnt(6)
	v_mfma_f32_32x32x16_bf16 v[20:35], v[72:75], v[204:207], v[20:35]
	v_mfma_f32_32x32x16_bf16 v[4:19], v[136:139], v[204:207], v[4:19]
	s_waitcnt lgkmcnt(5)
	v_mfma_f32_32x32x16_bf16 v[20:35], v[76:79], v[208:211], v[20:35]
	v_mfma_f32_32x32x16_bf16 v[4:19], v[140:143], v[208:211], v[4:19]
	s_waitcnt lgkmcnt(4)
	v_mfma_f32_32x32x16_bf16 v[20:35], v[80:83], v[212:215], v[20:35]
	v_mfma_f32_32x32x16_bf16 v[4:19], v[144:147], v[212:215], v[4:19]
	s_waitcnt lgkmcnt(3)
	v_mfma_f32_32x32x16_bf16 v[20:35], v[84:87], v[216:219], v[20:35]
	v_mfma_f32_32x32x16_bf16 v[4:19], v[148:151], v[216:219], v[4:19]
	s_waitcnt lgkmcnt(2)
	v_mfma_f32_32x32x16_bf16 v[20:35], v[88:91], v[220:223], v[20:35]
	v_mfma_f32_32x32x16_bf16 v[4:19], v[152:155], v[220:223], v[4:19]
	s_waitcnt lgkmcnt(1)
	v_mfma_f32_32x32x16_bf16 v[20:35], v[92:95], v[224:227], v[20:35]
	v_mfma_f32_32x32x16_bf16 v[4:19], v[160:163], v[224:227], v[4:19]
	s_waitcnt lgkmcnt(0)
	v_mfma_f32_32x32x16_bf16 v[20:35], v[96:99], v[228:231], v[20:35]
	v_mfma_f32_32x32x16_bf16 v[4:19], v[164:167], v[228:231], v[4:19]
	s_nop 10
	v_cvt_pk_bf16_f32 v20, v20, v21
	v_cvt_pk_bf16_f32 v21, v22, v23
	v_cvt_pk_bf16_f32 v22, v24, v25
	v_lshl_add_u64 v[24:25], v[196:197], 4, v[188:189]
	v_cvt_pk_bf16_f32 v23, v26, v27
	v_permlane32_swap_b32_e32 v20, v22
	v_cvt_pk_bf16_f32 v4, v4, v5
	v_cvt_pk_bf16_f32 v5, v6, v7
	v_cvt_pk_bf16_f32 v6, v8, v9
	v_cvt_pk_bf16_f32 v7, v10, v11
	v_add_co_u32_e32 v8, vcc, s25, v24
	v_permlane32_swap_b32_e32 v21, v23
	v_permlane32_swap_b32_e32 v4, v6
	v_permlane32_swap_b32_e32 v5, v7
	v_addc_co_u32_e32 v9, vcc, 0, v25, vcc
	global_store_dwordx4 v[24:25], v[20:23], off nt
	global_store_dwordx4 v[8:9], v[4:7], off nt
	s_and_b64 vcc, exec, s[38:39]
	v_cvt_pk_bf16_f32 v20, v28, v29
	v_cvt_pk_bf16_f32 v21, v30, v31
	v_cvt_pk_bf16_f32 v22, v32, v33
	v_cvt_pk_bf16_f32 v23, v34, v35
	v_cvt_pk_bf16_f32 v4, v12, v13
	v_cvt_pk_bf16_f32 v5, v14, v15
	v_cvt_pk_bf16_f32 v6, v16, v17
	v_cvt_pk_bf16_f32 v7, v18, v19
	v_permlane32_swap_b32_e32 v20, v22
	v_permlane32_swap_b32_e32 v21, v23
	v_permlane32_swap_b32_e32 v4, v6
	v_permlane32_swap_b32_e32 v5, v7
	global_store_dwordx4 v[24:25], v[20:23], off offset:2048 nt
	global_store_dwordx4 v[8:9], v[4:7], off offset:2048 nt
	s_cbranch_vccz .LBB0_974
	s_xor_b32 s9, s9, 1
	s_and_b64 vcc, exec, s[14:15]
	s_cbranch_vccz .LBB0_970
	s_mul_i32 s4, s9, 0x8400
	v_add_u32_e32 v2, s4, v181
	s_waitcnt vmcnt(7)
	ds_write_b128 v2, v[156:159]
	s_waitcnt vmcnt(6)
	ds_write_b128 v2, v[168:171] offset:8448
	s_waitcnt vmcnt(5)
	ds_write_b128 v2, v[172:175] offset:16896
	s_waitcnt vmcnt(4)
	ds_write_b128 v2, v[176:179] offset:25344
	s_branch .LBB0_970

.LBB0_1121:
	s_lshl_b32 s4, s63, 8
	v_mov_b32_e32 v108, v0
	s_add_i32 s4, s4, s58
	v_and_b32_e32 v198, 64, v250
	v_and_or_b32 v216, v108, 15, s4
	s_lshl_b32 s4, s56, 8
	v_bfe_u32 v196, v108, 4, 2
	s_or_b32 s4, s4, s59
	v_lshl_or_b32 v214, v196, 3, s4
	v_ashrrev_i32_e32 v215, 31, v214
	v_ashrrev_i32_e32 v217, 31, v216
	v_lshlrev_b64 v[232:233], 1, v[214:215]
	v_lshl_add_u64 v[118:119], s[14:15], 0, v[232:233]
	v_lshlrev_b64 v[234:235], 11, v[216:217]
	v_lshl_add_u64 v[128:129], v[118:119], 0, v[234:235]
	global_load_dwordx4 v[192:195], v[128:129], off nt
	global_load_dwordx4 v[188:191], v[128:129], off offset:256 nt
	v_or_b32_e32 v228, 16, v216
	v_ashrrev_i32_e32 v229, 31, v228
	v_or_b32_e32 v224, 32, v216
	v_ashrrev_i32_e32 v225, 31, v224
	v_or_b32_e32 v220, 48, v216
	v_lshlrev_b64 v[230:231], 11, v[228:229]
	v_ashrrev_i32_e32 v221, 31, v220
	v_lshl_add_u64 v[128:129], v[118:119], 0, v[230:231]
	v_lshlrev_b64 v[226:227], 11, v[224:225]
	v_add_u32_e32 v218, 0x80, v216
	v_add_u32_e32 v108, 0x90, v216
	global_load_dwordx4 v[184:187], v[128:129], off nt
	global_load_dwordx4 v[180:183], v[128:129], off offset:256 nt
	v_lshl_add_u64 v[128:129], v[118:119], 0, v[226:227]
	v_lshlrev_b64 v[222:223], 11, v[220:221]
	v_ashrrev_i32_e32 v219, 31, v218
	v_ashrrev_i32_e32 v109, 31, v108
	global_load_dwordx4 v[176:179], v[128:129], off nt
	global_load_dwordx4 v[172:175], v[128:129], off offset:256 nt
	v_lshl_add_u64 v[128:129], v[118:119], 0, v[222:223]
	v_add_u32_e32 v110, 0xa0, v216
	global_load_dwordx4 v[168:171], v[128:129], off nt
	global_load_dwordx4 v[164:167], v[128:129], off offset:256 nt
	v_lshlrev_b64 v[128:129], 11, v[218:219]
	v_lshlrev_b64 v[108:109], 11, v[108:109]
	v_ashrrev_i32_e32 v111, 31, v110
	v_lshl_add_u64 v[128:129], v[118:119], 0, v[128:129]
	v_lshl_add_u64 v[108:109], v[118:119], 0, v[108:109]
	v_add_u32_e32 v116, 0xb0, v216
	global_load_dwordx4 v[160:163], v[128:129], off nt
	global_load_dwordx4 v[156:159], v[128:129], off offset:256 nt
	global_load_dwordx4 v[152:155], v[108:109], off nt
	global_load_dwordx4 v[148:151], v[108:109], off offset:256 nt
	v_lshlrev_b64 v[108:109], 11, v[110:111]
	v_ashrrev_i32_e32 v117, 31, v116
	v_lshl_add_u64 v[108:109], v[118:119], 0, v[108:109]
	global_load_dwordx4 v[136:139], v[108:109], off nt
	global_load_dwordx4 v[128:131], v[108:109], off offset:256 nt
	v_lshlrev_b64 v[108:109], 11, v[116:117]
	v_lshl_add_u64 v[108:109], v[118:119], 0, v[108:109]
	global_load_dwordx4 v[116:119], v[108:109], off nt
	s_nop 0
	global_load_dwordx4 v[108:111], v[108:109], off offset:256 nt
	v_xor_b32_e32 v197, 16, v250
	v_add_u32_e32 v198, 64, v198
	v_cmp_lt_i32_e32 vcc, v197, v198
	s_lshl_b32 s44, s56, 2
	s_ashr_i32 s45, s44, 31
	v_cndmask_b32_e32 v197, v250, v197, vcc
	v_lshlrev_b32_e32 v237, 2, v197
	v_xor_b32_e32 v197, 32, v250
	v_cmp_lt_i32_e32 vcc, v197, v198
	s_waitcnt vmcnt(0)
	v_lshlrev_b32_e32 v198, 16, v194
	v_cndmask_b32_e32 v197, v250, v197, vcc
	v_lshlrev_b32_e32 v238, 2, v197
	v_cmp_eq_u32_e32 vcc, 0, v196
	v_lshlrev_b32_e32 v196, 16, v192
	v_and_b32_e32 v197, 0xffff0000, v192
	v_lshlrev_b32_e32 v192, 16, v193
	v_and_b32_e32 v193, 0xffff0000, v193
	v_and_b32_e32 v199, 0xffff0000, v194
	v_lshlrev_b32_e32 v194, 16, v195
	v_and_b32_e32 v195, 0xffff0000, v195
	v_pk_add_f32 v[144:145], v[144:145], v[196:197]
	v_pk_add_f32 v[146:147], v[146:147], v[192:193]
	v_pk_add_f32 v[192:193], v[142:143], v[194:195]
	v_pk_add_f32 v[142:143], v[140:141], v[198:199]
	v_cvt_pk_bf16_f32 v140, v144, v145
	v_lshl_add_u64 v[144:145], s[14:15], 0, v[234:235]
	v_cvt_pk_bf16_f32 v141, v146, v147
	v_cvt_pk_bf16_f32 v142, v142, v143
	v_cvt_pk_bf16_f32 v143, v192, v193
	v_lshl_add_u64 v[144:145], v[144:145], 0, v[232:233]
	global_store_dwordx4 v[144:145], v[140:143], off
	v_lshlrev_b32_e32 v146, 16, v140
	v_lshlrev_b32_e32 v147, 16, v141
	v_and_b32_e32 v140, 0xffff0000, v140
	v_and_b32_e32 v141, 0xffff0000, v141
	v_mul_f32_e32 v140, v140, v140
	v_mul_f32_e32 v141, v141, v141
	v_lshlrev_b32_e32 v192, 16, v142
	v_and_b32_e32 v142, 0xffff0000, v142
	v_lshlrev_b32_e32 v193, 16, v143
	v_and_b32_e32 v143, 0xffff0000, v143
	v_fmac_f32_e32 v140, v146, v146
	v_fmac_f32_e32 v141, v147, v147
	v_add_f32_e32 v140, v140, v141
	v_mul_f32_e32 v141, v142, v142
	v_mul_f32_e32 v142, v143, v143
	v_fmac_f32_e32 v141, v192, v192
	v_fmac_f32_e32 v142, v193, v193
	v_add_f32_e32 v141, v141, v142
	v_add_f32_e32 v192, v140, v141
	v_lshlrev_b32_e32 v140, 16, v188
	v_and_b32_e32 v141, 0xffff0000, v188
	v_lshlrev_b32_e32 v142, 16, v189
	v_and_b32_e32 v143, 0xffff0000, v189
	v_lshlrev_b32_e32 v146, 16, v190
	v_and_b32_e32 v147, 0xffff0000, v190
	v_lshlrev_b32_e32 v188, 16, v191
	v_and_b32_e32 v189, 0xffff0000, v191
	v_pk_add_f32 v[134:135], v[134:135], v[142:143]
	v_pk_add_f32 v[132:133], v[132:133], v[140:141]
	v_pk_add_f32 v[140:141], v[126:127], v[188:189]
	v_pk_add_f32 v[126:127], v[124:125], v[146:147]
	v_cvt_pk_bf16_f32 v124, v132, v133
	v_cvt_pk_bf16_f32 v125, v134, v135
	v_cvt_pk_bf16_f32 v126, v126, v127
	v_cvt_pk_bf16_f32 v127, v140, v141
	global_store_dwordx4 v[144:145], v[124:127], off offset:256
	v_lshlrev_b32_e32 v132, 16, v124
	v_lshlrev_b32_e32 v133, 16, v125
	v_and_b32_e32 v124, 0xffff0000, v124
	v_and_b32_e32 v125, 0xffff0000, v125
	v_mul_f32_e32 v124, v124, v124
	v_mul_f32_e32 v125, v125, v125
	v_lshlrev_b32_e32 v134, 16, v126
	v_and_b32_e32 v126, 0xffff0000, v126
	v_lshlrev_b32_e32 v135, 16, v127
	v_and_b32_e32 v127, 0xffff0000, v127
	v_fmac_f32_e32 v124, v132, v132
	v_fmac_f32_e32 v125, v133, v133
	v_add_f32_e32 v124, v124, v125
	v_mul_f32_e32 v125, v126, v126
	v_mul_f32_e32 v126, v127, v127
	v_fmac_f32_e32 v125, v134, v134
	v_fmac_f32_e32 v126, v135, v135
	v_add_f32_e32 v125, v125, v126
	v_add_f32_e32 v124, v124, v125
	v_add_f32_e32 v124, v192, v124
	ds_bpermute_b32 v125, v237, v124
	s_waitcnt lgkmcnt(0)
	v_add_f32_e32 v124, v124, v125
	ds_bpermute_b32 v125, v238, v124
	s_and_saveexec_b64 s[4:5], vcc
	s_cbranch_execz .LBB0_1123
	v_lshlrev_b64 v[126:127], 6, v[216:217]
	v_lshl_add_u64 v[126:127], s[18:19], 0, v[126:127]
	v_lshl_add_u64 v[126:127], s[44:45], 2, v[126:127]
	s_lshl_b32 s56, s53, 2
	v_lshl_add_u64 v[126:127], v[126:127], 0, s[56:57]
	s_waitcnt lgkmcnt(0)
	v_add_f32_e32 v124, v124, v125
	global_store_dword v[126:127], v124, off

.LBB0_1462:
	s_lshl_b32 s4, s65, 8
	v_mov_b32_e32 v112, v0
	s_add_i32 s4, s4, s60
	v_and_b32_e32 v198, 64, v250
	v_and_or_b32 v216, v112, 15, s4
	v_ashrrev_i32_e32 v217, 31, v216
	v_bfe_u32 v196, v112, 4, 2
	v_lshl_add_u64 v[112:113], v[216:217], 2, s[20:21]
	global_load_dword v114, v[112:113], off nt
	global_load_dword v243, v[112:113], off offset:512 nt
	v_or_b32_e32 v226, 16, v216
	v_ashrrev_i32_e32 v227, 31, v226
	v_or_b32_e32 v222, 32, v216
	v_ashrrev_i32_e32 v223, 31, v222
	v_or_b32_e32 v220, 48, v216
	v_ashrrev_i32_e32 v221, 31, v220
	v_add_u32_e32 v112, 0x90, v216
	v_ashrrev_i32_e32 v113, 31, v112
	s_lshl_b32 s4, s56, 8
	s_or_b32 s4, s4, s61
	v_lshl_or_b32 v214, v196, 3, s4
	v_ashrrev_i32_e32 v215, 31, v214
	v_lshlrev_b64 v[234:235], 1, v[214:215]
	v_lshlrev_b64 v[236:237], 11, v[216:217]
	v_lshlrev_b64 v[230:231], 11, v[226:227]
	v_lshlrev_b64 v[228:229], 11, v[222:223]
	v_add_u32_e32 v218, 0x80, v216
	v_lshlrev_b64 v[224:225], 11, v[220:221]
	v_ashrrev_i32_e32 v219, 31, v218
	v_xor_b32_e32 v197, 16, v250
	v_add_u32_e32 v198, 64, v198
	v_cmp_lt_i32_e32 vcc, v197, v198
	s_lshl_b32 s48, s56, 2
	s_ashr_i32 s49, s48, 31
	v_cndmask_b32_e32 v197, v250, v197, vcc
	v_lshlrev_b32_e32 v240, 2, v197
	v_xor_b32_e32 v197, 32, v250
	v_cmp_lt_i32_e32 vcc, v197, v198
	s_waitcnt vmcnt(0)
	v_mul_f32_e32 v232, v114, v114
	v_lshl_add_u64 v[114:115], v[226:227], 2, s[20:21]
	global_load_dword v246, v[114:115], off nt
	v_lshl_add_u64 v[114:115], v[222:223], 2, s[20:21]
	global_load_dword v245, v[114:115], off nt
	v_lshl_add_u64 v[114:115], v[220:221], 2, s[20:21]
	global_load_dword v244, v[114:115], off nt
	v_lshl_add_u64 v[114:115], v[112:113], 2, s[20:21]
	global_load_dword v242, v[114:115], off nt
	v_add_u32_e32 v114, 0xa0, v216
	v_ashrrev_i32_e32 v115, 31, v114
	v_lshl_add_u64 v[120:121], v[114:115], 2, s[20:21]
	global_load_dword v239, v[120:121], off nt
	v_add_u32_e32 v120, 0xb0, v216
	v_ashrrev_i32_e32 v121, 31, v120
	v_lshl_add_u64 v[122:123], v[120:121], 2, s[20:21]
	global_load_dword v238, v[122:123], off nt
	v_lshl_add_u64 v[122:123], s[14:15], 0, v[234:235]
	v_lshl_add_u64 v[132:133], v[122:123], 0, v[236:237]
	global_load_dwordx4 v[192:195], v[132:133], off nt
	global_load_dwordx4 v[188:191], v[132:133], off offset:256 nt
	v_lshl_add_u64 v[132:133], v[122:123], 0, v[230:231]
	global_load_dwordx4 v[184:187], v[132:133], off nt
	global_load_dwordx4 v[180:183], v[132:133], off offset:256 nt
	v_lshl_add_u64 v[132:133], v[122:123], 0, v[228:229]
	global_load_dwordx4 v[176:179], v[132:133], off nt
	global_load_dwordx4 v[172:175], v[132:133], off offset:256 nt
	v_lshl_add_u64 v[132:133], v[122:123], 0, v[224:225]
	global_load_dwordx4 v[168:171], v[132:133], off nt
	global_load_dwordx4 v[164:167], v[132:133], off offset:256 nt
	v_lshlrev_b64 v[132:133], 11, v[218:219]
	v_lshlrev_b64 v[112:113], 11, v[112:113]
	v_lshl_add_u64 v[132:133], v[122:123], 0, v[132:133]
	v_lshl_add_u64 v[112:113], v[122:123], 0, v[112:113]
	global_load_dwordx4 v[160:163], v[132:133], off nt
	global_load_dwordx4 v[156:159], v[132:133], off offset:256 nt
	global_load_dwordx4 v[152:155], v[112:113], off nt
	global_load_dwordx4 v[148:151], v[112:113], off offset:256 nt
	v_lshlrev_b64 v[112:113], 11, v[114:115]
	v_lshl_add_u64 v[112:113], v[122:123], 0, v[112:113]
	global_load_dwordx4 v[144:147], v[112:113], off nt
	global_load_dwordx4 v[132:135], v[112:113], off offset:256 nt
	v_lshlrev_b64 v[112:113], 11, v[120:121]
	v_lshl_add_u64 v[112:113], v[122:123], 0, v[112:113]
	global_load_dwordx4 v[120:123], v[112:113], off nt
	s_nop 0
	global_load_dwordx4 v[112:115], v[112:113], off offset:256 nt
	v_cndmask_b32_e32 v197, v250, v197, vcc
	v_lshlrev_b32_e32 v241, 2, v197
	v_cmp_eq_u32_e32 vcc, 0, v196
	s_waitcnt vmcnt(15)
	v_lshlrev_b32_e32 v196, 16, v192
	v_and_b32_e32 v197, 0xffff0000, v192
	v_lshlrev_b32_e32 v192, 16, v193
	v_and_b32_e32 v193, 0xffff0000, v193
	v_lshlrev_b32_e32 v198, 16, v194
	v_and_b32_e32 v199, 0xffff0000, v194
	v_lshlrev_b32_e32 v194, 16, v195
	v_and_b32_e32 v195, 0xffff0000, v195
	v_pk_fma_f32 v[140:141], v[140:141], v[232:233], v[196:197] op_sel_hi:[1,0,1]
	v_pk_fma_f32 v[142:143], v[142:143], v[232:233], v[192:193] op_sel_hi:[1,0,1]
	v_pk_fma_f32 v[192:193], v[138:139], v[232:233], v[194:195] op_sel_hi:[1,0,1]
	v_pk_fma_f32 v[138:139], v[136:137], v[232:233], v[198:199] op_sel_hi:[1,0,1]
	v_cvt_pk_bf16_f32 v136, v140, v141
	v_lshl_add_u64 v[140:141], s[14:15], 0, v[236:237]
	v_cvt_pk_bf16_f32 v137, v142, v143
	v_cvt_pk_bf16_f32 v138, v138, v139
	v_cvt_pk_bf16_f32 v139, v192, v193
	v_lshl_add_u64 v[140:141], v[140:141], 0, v[234:235]
	global_store_dwordx4 v[140:141], v[136:139], off
	v_lshlrev_b32_e32 v142, 16, v136
	v_lshlrev_b32_e32 v143, 16, v137
	v_and_b32_e32 v136, 0xffff0000, v136
	v_and_b32_e32 v137, 0xffff0000, v137
	v_mul_f32_e32 v136, v136, v136
	v_mul_f32_e32 v137, v137, v137
	v_lshlrev_b32_e32 v192, 16, v138
	v_and_b32_e32 v138, 0xffff0000, v138
	v_lshlrev_b32_e32 v193, 16, v139
	v_and_b32_e32 v139, 0xffff0000, v139
	v_fmac_f32_e32 v136, v142, v142
	v_fmac_f32_e32 v137, v143, v143
	v_add_f32_e32 v136, v136, v137
	v_mul_f32_e32 v137, v138, v138
	v_mul_f32_e32 v138, v139, v139
	v_fmac_f32_e32 v137, v192, v192
	v_fmac_f32_e32 v138, v193, v193
	v_add_f32_e32 v137, v137, v138
	v_add_f32_e32 v192, v136, v137
	s_waitcnt vmcnt(15)
	v_lshlrev_b32_e32 v136, 16, v188
	v_and_b32_e32 v137, 0xffff0000, v188
	v_lshlrev_b32_e32 v138, 16, v189
	v_and_b32_e32 v139, 0xffff0000, v189
	v_lshlrev_b32_e32 v142, 16, v190
	v_and_b32_e32 v143, 0xffff0000, v190
	v_lshlrev_b32_e32 v188, 16, v191
	v_and_b32_e32 v189, 0xffff0000, v191
	v_pk_fma_f32 v[130:131], v[130:131], v[232:233], v[138:139] op_sel_hi:[1,0,1]
	v_pk_fma_f32 v[128:129], v[128:129], v[232:233], v[136:137] op_sel_hi:[1,0,1]
	v_pk_fma_f32 v[136:137], v[126:127], v[232:233], v[188:189] op_sel_hi:[1,0,1]
	v_pk_fma_f32 v[126:127], v[124:125], v[232:233], v[142:143] op_sel_hi:[1,0,1]
	v_cvt_pk_bf16_f32 v124, v128, v129
	v_cvt_pk_bf16_f32 v125, v130, v131
	v_cvt_pk_bf16_f32 v126, v126, v127
	v_cvt_pk_bf16_f32 v127, v136, v137
	global_store_dwordx4 v[140:141], v[124:127], off offset:256
	v_lshlrev_b32_e32 v128, 16, v124
	v_lshlrev_b32_e32 v129, 16, v125
	v_and_b32_e32 v124, 0xffff0000, v124
	v_and_b32_e32 v125, 0xffff0000, v125
	v_mul_f32_e32 v124, v124, v124
	v_mul_f32_e32 v125, v125, v125
	v_lshlrev_b32_e32 v130, 16, v126
	v_and_b32_e32 v126, 0xffff0000, v126
	v_lshlrev_b32_e32 v131, 16, v127
	v_and_b32_e32 v127, 0xffff0000, v127
	v_fmac_f32_e32 v124, v128, v128
	v_fmac_f32_e32 v125, v129, v129
	v_add_f32_e32 v124, v124, v125
	v_mul_f32_e32 v125, v126, v126
	v_mul_f32_e32 v126, v127, v127
	v_fmac_f32_e32 v125, v130, v130
	v_fmac_f32_e32 v126, v131, v131
	v_add_f32_e32 v125, v125, v126
	v_add_f32_e32 v124, v124, v125
	v_add_f32_e32 v124, v192, v124
	ds_bpermute_b32 v125, v240, v124
	s_waitcnt lgkmcnt(0)
	v_add_f32_e32 v124, v124, v125
	ds_bpermute_b32 v125, v241, v124
	s_and_saveexec_b64 s[4:5], vcc
	v_readlane_b32 s74, v255, 38
	s_cbranch_execz .LBB0_1464
	v_lshlrev_b64 v[126:127], 6, v[216:217]
	v_lshl_add_u64 v[126:127], s[18:19], 0, v[126:127]
	v_lshl_add_u64 v[126:127], s[48:49], 2, v[126:127]
	s_lshl_b32 s56, s59, 2
	v_lshl_add_u64 v[126:127], v[126:127], 0, s[56:57]
	s_waitcnt lgkmcnt(0)
	v_add_f32_e32 v124, v124, v125
	global_store_dword v[126:127], v124, off

.LBB0_1534:
	s_add_u32 s0, s8, s2
	s_addc_u32 s1, s9, s3
	s_add_u32 s10, s0, 0x1f800000
	s_addc_u32 s11, s1, 0
	v_lshl_add_u64 v[30:31], v[4:5], 0, s[2:3]
	global_load_dwordx4 v[10:13], v[2:3], off nt
	global_load_dwordx4 v[14:17], v0, s[0:1] nt
	global_load_dwordx4 v[18:21], v1, s[10:11] offset:48 nt
	global_load_dwordx4 v[22:25], v1, s[10:11] offset:32 nt
	global_load_dwordx4 v[26:29], v1, s[10:11] offset:16 nt
	global_load_dwordx2 v[32:33], v[30:31], off offset:-1024 nt
	s_add_i32 s4, s4, s90
	s_add_u32 s8, s8, s6
	s_addc_u32 s9, s9, s7
	v_lshl_add_u64 v[4:5], v[4:5], 0, s[14:15]
	s_cmp_lt_i32 s4, 0x8000
	s_waitcnt vmcnt(0)
	v_add_f32_e32 v22, v22, v23
	v_add_f32_e32 v24, v24, v25
	v_lshlrev_b32_e32 v34, 16, v32
	v_and_b32_e32 v35, 0xffff0000, v32
	v_lshlrev_b32_e32 v36, 16, v33
	v_and_b32_e32 v37, 0xffff0000, v33
	v_mov_b32_e32 v32, v15
	v_mov_b32_e32 v33, v16
	v_mov_b32_e32 v15, v17
	v_mov_b32_e32 v16, v27
	v_mov_b32_e32 v17, v28
	v_mov_b32_e32 v27, v29
	v_pk_add_f32 v[14:15], v[32:33], v[14:15]
	v_pk_add_f32 v[16:17], v[16:17], v[26:27]
	v_pk_add_f32 v[14:15], v[14:15], v[14:15] op_sel:[0,1] op_sel_hi:[1,0]
	v_pk_add_f32 v[16:17], v[16:17], v[16:17] op_sel:[0,1] op_sel_hi:[1,0]
	v_mov_b32_e32 v23, v20
	v_mov_b32_e32 v25, v21
	v_mov_b32_e32 v15, v18
	v_mov_b32_e32 v17, v19
	v_pk_add_f32 v[20:21], v[22:23], v[24:25]
	v_pk_add_f32 v[14:15], v[14:15], v[16:17]
	s_nop 0
	v_pk_add_f32 v[14:15], v[14:15], v[20:21]
	s_nop 0
	v_add_f32_e32 v14, v14, v15
	v_fmamk_f32 v14, v14, 0x3a800000, v8
	v_mul_f32_e32 v15, 0x4f800000, v14
	v_cmp_gt_f32_e32 vcc, s5, v14
	s_nop 1
	v_cndmask_b32_e32 v14, v14, v15, vcc
	v_sqrt_f32_e32 v15, v14
	s_nop 0
	v_add_u32_e32 v16, -1, v15
	v_add_u32_e32 v17, 1, v15
	v_fma_f32 v18, -v16, v15, v14
	v_fma_f32 v19, -v17, v15, v14
	v_cmp_ge_f32_e64 s[0:1], 0, v18
	s_nop 1
	v_cndmask_b32_e64 v15, v15, v16, s[0:1]
	v_cmp_lt_f32_e64 s[0:1], 0, v19
	s_nop 1
	v_cndmask_b32_e64 v15, v15, v17, s[0:1]
	v_mul_f32_e32 v16, 0x37800000, v15
	v_cndmask_b32_e32 v15, v15, v16, vcc
	v_cmp_class_f32_e32 vcc, v14, v9
	s_nop 1
	v_cndmask_b32_e32 v14, v15, v14, vcc
	v_div_scale_f32 v15, s[0:1], v14, v14, 1.0
	v_rcp_f32_e32 v17, v15
	v_div_scale_f32 v16, vcc, 1.0, v14, 1.0
	v_fma_f32 v18, -v15, v17, 1.0
	v_fmac_f32_e32 v17, v18, v17
	v_mul_f32_e32 v18, v16, v17
	v_fma_f32 v19, -v15, v18, v16
	v_fmac_f32_e32 v18, v19, v17
	v_fma_f32 v15, -v15, v18, v16
	v_div_fmas_f32 v15, v15, v17, v18
	v_div_fixup_f32 v16, v15, v14, 1.0
	v_mul_f32_e32 v14, v16, v34
	v_mul_f32_e32 v15, v16, v35
	v_mul_f32_e32 v17, v16, v36
	v_mul_f32_e32 v18, v16, v37
	v_mul_f32_e32 v10, v10, v14
	v_mul_f32_e32 v11, v11, v15
	v_mul_f32_e32 v12, v12, v17
	v_mul_f32_e32 v13, v13, v18
	global_store_dwordx4 v[6:7], v[10:13], off offset:-2048 nt
	global_load_dwordx2 v[14:15], v[30:31], off offset:-512 nt
	s_nop 0
	global_load_dwordx4 v[10:13], v[2:3], off offset:1024 nt
	s_waitcnt vmcnt(1)
	v_lshlrev_b32_e32 v17, 16, v14
	v_and_b32_e32 v14, 0xffff0000, v14
	v_lshlrev_b32_e32 v18, 16, v15
	v_and_b32_e32 v15, 0xffff0000, v15
	v_mul_f32_e32 v17, v16, v17
	v_mul_f32_e32 v14, v16, v14
	v_mul_f32_e32 v18, v16, v18
	v_mul_f32_e32 v15, v16, v15
	s_waitcnt vmcnt(0)
	v_mul_f32_e32 v10, v10, v17
	v_mul_f32_e32 v11, v11, v14
	v_mul_f32_e32 v12, v12, v18
	v_mul_f32_e32 v13, v13, v15
	global_store_dwordx4 v[6:7], v[10:13], off offset:-1024 nt
	global_load_dwordx2 v[14:15], v[30:31], off nt
	s_nop 0
	global_load_dwordx4 v[10:13], v[2:3], off offset:2048 nt
	s_waitcnt vmcnt(1)
	v_lshlrev_b32_e32 v17, 16, v14
	v_and_b32_e32 v14, 0xffff0000, v14
	v_lshlrev_b32_e32 v18, 16, v15
	v_and_b32_e32 v15, 0xffff0000, v15
	v_mul_f32_e32 v17, v16, v17
	v_mul_f32_e32 v14, v16, v14
	v_mul_f32_e32 v18, v16, v18
	v_mul_f32_e32 v15, v16, v15
	s_waitcnt vmcnt(0)
	v_mul_f32_e32 v10, v10, v17
	v_mul_f32_e32 v11, v11, v14
	v_mul_f32_e32 v12, v12, v18
	v_mul_f32_e32 v13, v13, v15
	global_store_dwordx4 v[6:7], v[10:13], off nt
	global_load_dwordx2 v[14:15], v[30:31], off offset:512 nt
	s_nop 0
	global_load_dwordx4 v[10:13], v[2:3], off offset:3072 nt
	s_waitcnt vmcnt(1)
	v_lshlrev_b32_e32 v17, 16, v14
	v_and_b32_e32 v14, 0xffff0000, v14
	v_lshlrev_b32_e32 v18, 16, v15
	v_and_b32_e32 v15, 0xffff0000, v15
	v_mul_f32_e32 v17, v16, v17
	v_mul_f32_e32 v14, v16, v14
	v_mul_f32_e32 v18, v16, v18
	v_mul_f32_e32 v15, v16, v15
	s_waitcnt vmcnt(0)
	v_mul_f32_e32 v10, v10, v17
	v_mul_f32_e32 v11, v11, v14
	v_mul_f32_e32 v12, v12, v18
	v_mul_f32_e32 v13, v13, v15
	global_store_dwordx4 v[6:7], v[10:13], off offset:1024 nt
	v_lshl_add_u64 v[6:7], v[6:7], 0, s[12:13]
	s_cbranch_scc1 .LBB0_1534
